# per-expert routing counters moved from 256 packed ints (32 per cache line) to unused zeroed words of the LayerNorm counter lines, 2 counters per 128B line: removes same-line atomic serialisation in th
# speedup vs baseline: 1.0949x; 1.0699x over previous
.LBB0_578:
	s_or_b64 exec, exec, s[0:1]
	s_add_u32 s40, s70, 0x5440
	s_addc_u32 s41, s71, 0
	s_add_u32 s0, s70, 0x1260d500
	s_addc_u32 s1, s71, 0
	v_writelane_b32 v253, s0, 55
	s_waitcnt lgkmcnt(0)
	s_barrier
	v_writelane_b32 v253, s1, 56
	s_add_u32 s0, s70, 0x1268d500
	s_addc_u32 s1, s71, 0
	v_writelane_b32 v253, s0, 57
	v_mov_b32_e32 v1, 0
	s_nop 0
	v_writelane_b32 v253, s1, 58
	s_add_u32 s0, s70, 0x1270d500
	s_addc_u32 s1, s71, 0
	v_writelane_b32 v253, s0, 59
	v_mov_b32_e32 v3, 0
	s_movk_i32 s33, 0x4000
	v_writelane_b32 v253, s1, 60
	s_add_u32 s0, s70, 0x1278d500
	s_addc_u32 s1, s71, 0
	v_writelane_b32 v253, s0, 61
	s_nop 1
	v_writelane_b32 v253, s1, 62
	s_getreg_b32 s0, hwreg(HW_REG_HW_ID, 0, 6)
	s_lshl_b32 s0, s0, 2
	s_add_i32 s0, s0, 0x27000
	v_mov_b32_e32 v0, s0
	ds_read_b32 v0, v0
	s_waitcnt lgkmcnt(0)
	v_readfirstlane_b32 s0, v0
	v_mbcnt_lo_u32_b32 v0, -1, v1
	v_mbcnt_hi_u32_b32 v0, -1, v0
	v_lshl_or_b32 v0, s0, 6, v0
	s_getreg_b32 s0, hwreg(HW_REG_HW_ID, 0, 6)
	s_lshl_b32 s0, s0, 2
	s_add_i32 s0, s0, 0x27000
	v_mov_b32_e32 v1, s0
	ds_read_b32 v2, v1
	v_mov_b32_e32 v1, 0
	s_waitcnt lgkmcnt(0)
	v_readfirstlane_b32 s0, v2
	v_mbcnt_lo_u32_b32 v2, -1, v3
	v_mbcnt_hi_u32_b32 v2, -1, v2
	v_lshl_or_b32 v2, s0, 6, v2
	v_readlane_b32 s0, v253, 30
	v_ashrrev_i32_e32 v8, 6, v2
	s_nop 0
	v_add_u32_e32 v2, s0, v8
	v_cmp_gt_i32_e32 vcc, s33, v2
	s_and_saveexec_b64 s[44:45], vcc
	s_cbranch_execz .LBB0_667
	v_ashrrev_i32_e32 v3, 31, v2
	v_readlane_b32 s2, v253, 53
	v_and_b32_e32 v22, 63, v0
	v_lshlrev_b64 v[4:5], 10, v[2:3]
	v_readlane_b32 s3, v253, 54
	v_lshlrev_b32_e32 v0, 2, v22
	v_readlane_b32 s12, v253, 4
	v_lshl_add_u64 v[4:5], s[2:3], 0, v[4:5]
	v_lshl_add_u64 v[4:5], v[4:5], 0, v[0:1]
	global_load_dword v24, v[4:5], off
	global_load_dword v29, v[4:5], off offset:256
	global_load_dword v30, v[4:5], off offset:512
	global_load_dword v9, v[4:5], off offset:768
	v_readlane_b32 s13, v253, 5
	v_xor_b32_e32 v3, 64, v0
	v_xor_b32_e32 v23, 0x80, v0
	v_lshl_add_u64 v[4:5], s[12:13], 0, v[0:1]
	v_lshl_add_u64 v[6:7], s[2:3], 0, v[0:1]
	s_lshl_b32 s2, s72, 6
	v_lshlrev_b32_e32 v0, 3, v8
	v_readlane_b32 s14, v253, 6
	v_readlane_b32 s15, v253, 7
	v_readlane_b32 s16, v253, 8
	v_readlane_b32 s17, v253, 9
	v_readlane_b32 s18, v253, 10
	v_readlane_b32 s19, v253, 11
	v_readlane_b32 s20, v253, 12
	v_readlane_b32 s21, v253, 13
	v_readlane_b32 s22, v253, 14
	v_readlane_b32 s23, v253, 15
	v_readlane_b32 s24, v253, 16
	v_readlane_b32 s25, v253, 17
	v_add3_u32 v8, s2, v0, v22
	v_readlane_b32 s2, v253, 2
	v_cmp_gt_u32_e64 s[0:1], 32, v22
	v_cmp_lt_u32_e64 s[4:5], 31, v22
	v_cmp_lt_u32_e64 s[6:7], 7, v22
	v_cmp_gt_u32_e64 s[8:9], 8, v22
	v_cmp_eq_u32_e64 s[10:11], 0, v22
	v_cmp_eq_u32_e64 s[12:13], 1, v22
	v_cmp_eq_u32_e64 s[14:15], 2, v22
	v_cmp_eq_u32_e64 s[16:17], 3, v22
	v_cmp_eq_u32_e64 s[18:19], 4, v22
	v_cmp_eq_u32_e64 s[20:21], 5, v22
	v_cmp_eq_u32_e64 s[22:23], 6, v22
	v_cmp_eq_u32_e64 s[24:25], 7, v22
	s_lshl_b32 s52, s2, 6
	s_mov_b64 s[46:47], 0
	s_mov_b32 s53, 0xbfb8aa3b
	s_mov_b32 s54, 0x42ce8ed0
	s_mov_b32 s55, 0xc2b17218
	v_mov_b32_e32 v25, 0x7f800000
	v_mov_b32_e32 v26, 0xff800000
	v_mov_b32_e32 v27, 1
	v_readlane_b32 s26, v253, 18
	v_readlane_b32 s27, v253, 19
	v_readlane_b32 s3, v253, 3
	s_branch .LBB0_581

.LBB0_657:
	v_mov_b32_e32 v0, s56
	v_cndmask_b32_e64 v0, 0, v0, s[10:11]
	v_mov_b32_e32 v9, s57
	v_cndmask_b32_e64 v0, v0, v9, s[12:13]
	v_mov_b32_e32 v9, s58
	v_cndmask_b32_e64 v0, v0, v9, s[14:15]
	v_mov_b32_e32 v9, s59
	v_cndmask_b32_e64 v0, v0, v9, s[16:17]
	v_mov_b32_e32 v9, s60
	v_cndmask_b32_e64 v0, v0, v9, s[18:19]
	v_mov_b32_e32 v9, s61
	v_cndmask_b32_e64 v0, v0, v9, s[20:21]
	v_mov_b32_e32 v9, s62
	v_cndmask_b32_e64 v0, v0, v9, s[22:23]
	v_mov_b32_e32 v9, s63
	v_cndmask_b32_e64 v0, v0, v9, s[24:25]
	v_lshlrev_b32_e32 v9, 2, v0
	v_and_b32_e32 v9, 0xfc, v9
	ds_bpermute_b32 v12, v9, v12
	ds_bpermute_b32 v13, v9, v13
	ds_bpermute_b32 v11, v9, v11
	ds_bpermute_b32 v9, v9, v10
	v_lshrrev_b32_e32 v14, 6, v0
	v_cmp_eq_u32_e32 vcc, 2, v14
	s_waitcnt lgkmcnt(2)
	s_nop 0
	v_cndmask_b32_e32 v10, v13, v12, vcc
	v_cmp_eq_u32_e32 vcc, 1, v14
	s_waitcnt lgkmcnt(1)
	s_nop 0
	v_cndmask_b32_e32 v10, v10, v11, vcc
	v_cmp_gt_u32_e32 vcc, 64, v0
	s_waitcnt lgkmcnt(0)
	s_nop 0
	v_cndmask_b32_e32 v10, v10, v9, vcc
	v_cndmask_b32_e64 v9, v10, 0, s[6:7]
	s_nop 1
	v_add_f32_dpp v9, v9, v9 quad_perm:[1,0,3,2] row_mask:0xf bank_mask:0xf bound_ctrl:1
	s_nop 1
	v_add_f32_dpp v9, v9, v9 quad_perm:[2,3,0,1] row_mask:0xf bank_mask:0xf bound_ctrl:1
	s_nop 1
	v_mov_b32_dpp v11, v9 row_half_mirror row_mask:0xf bank_mask:0xf bound_ctrl:1
	s_and_saveexec_b64 s[2:3], s[8:9]
	s_cbranch_execz .LBB0_580
	v_lshlrev_b32_e32 v12, 6, v0
	v_and_b32_e32 v12, 0xffffff00, v12
	v_and_b32_e32 v13, 3, v0
	v_lshl_or_b32 v12, v13, 5, v12
	v_mov_b32_e32 v13, 0
	v_lshl_add_u64 v[12:13], v[12:13], 0, s[40:41]
	global_atomic_add v12, v[12:13], v27, off sc0
	v_add_f32_e32 v11, v9, v11
	v_ashrrev_i32_e32 v9, 31, v8
	v_readlane_b32 s28, v253, 55
	v_lshlrev_b64 v[14:15], 2, v[8:9]
	v_readlane_b32 s29, v253, 56
	s_nop 1
	v_lshl_add_u64 v[16:17], s[28:29], 0, v[14:15]
	v_readlane_b32 s28, v253, 59
	v_readlane_b32 s29, v253, 60
	global_store_dword v[16:17], v0, off
	s_nop 0
	v_lshl_add_u64 v[16:17], s[28:29], 0, v[14:15]
	v_div_scale_f32 v9, s[28:29], v11, v11, v10
	v_rcp_f32_e32 v13, v9
	v_readlane_b32 s28, v253, 57
	v_readlane_b32 s29, v253, 58
	s_waitcnt vmcnt(1)
	global_store_dword v[16:17], v12, off
	v_fma_f32 v16, -v9, v13, 1.0
	v_fmac_f32_e32 v13, v16, v13
	v_div_scale_f32 v16, vcc, v10, v11, v10
	v_mul_f32_e32 v17, v16, v13
	v_fma_f32 v18, -v9, v17, v16
	v_fmac_f32_e32 v17, v18, v13
	v_fma_f32 v9, -v9, v17, v16
	v_div_fmas_f32 v9, v9, v13, v17
	v_div_fixup_f32 v9, v9, v11, v10
	v_mul_f32_e32 v9, 0x40200000, v9
	v_lshl_add_u64 v[10:11], s[28:29], 0, v[14:15]
	v_readlane_b32 s28, v253, 61
	global_store_dword v[10:11], v9, off
	v_lshlrev_b64 v[10:11], 16, v[0:1]
	v_readlane_b32 s29, v253, 62
	v_ashrrev_i32_e32 v13, 31, v12
	s_nop 0
	v_lshl_add_u64 v[10:11], s[28:29], 0, v[10:11]
	v_lshl_add_u64 v[10:11], v[12:13], 2, v[10:11]
	global_store_dword v[10:11], v2, off
	s_branch .LBB0_580

.LBB0_719:
	s_or_b64 exec, exec, s[0:1]
	s_waitcnt lgkmcnt(0)
	s_barrier
	s_getreg_b32 s0, hwreg(HW_REG_HW_ID, 0, 6)
	s_lshl_b32 s0, s0, 2
	s_add_i32 s0, s0, 0x27000
	v_mov_b32_e32 v0, s0
	ds_read_b32 v0, v0
	v_mov_b32_e32 v1, 0
	v_mov_b32_e32 v2, 0
	s_waitcnt lgkmcnt(0)
	v_readfirstlane_b32 s0, v0
	v_mbcnt_lo_u32_b32 v0, -1, v1
	v_mbcnt_hi_u32_b32 v0, -1, v0
	s_waitcnt vmcnt(9)
	v_lshl_or_b32 v52, s0, 6, v0
	s_getreg_b32 s0, hwreg(HW_REG_HW_ID, 0, 6)
	s_lshl_b32 s0, s0, 2
	s_add_i32 s0, s0, 0x27000
	v_mov_b32_e32 v0, s0
	ds_read_b32 v0, v0
	v_mov_b32_e32 v1, 0
	s_waitcnt lgkmcnt(0)
	v_readfirstlane_b32 s0, v0
	v_mbcnt_lo_u32_b32 v0, -1, v2
	v_mbcnt_hi_u32_b32 v0, -1, v0
	v_lshl_or_b32 v0, s0, 6, v0
	s_movk_i32 s0, 0x100
	s_nop 0
	v_cmp_gt_i32_e32 vcc, s0, v0
	v_lshl_add_u32 v2, v0, 2, 0
	s_and_saveexec_b64 s[0:1], vcc
	s_cbranch_execz .LBB0_721
	v_ashrrev_i32_e32 v1, 31, v0
	v_lshlrev_b32_e32 v4, 6, v0
	v_and_b32_e32 v4, 0xffffff00, v4
	v_and_b32_e32 v5, 3, v0
	v_lshl_or_b32 v4, v5, 5, v4
	v_mov_b32_e32 v5, 0
	v_lshl_add_u64 v[4:5], v[4:5], 0, s[40:41]
	global_load_dword v1, v[4:5], off
	v_add_u32_e32 v3, 0x1e800, v2
	s_mov_b32 s2, 0x66666667
	s_waitcnt vmcnt(0)
	ds_write_b32 v3, v1
	v_add_u32_e32 v3, 0x13f, v1
	v_mul_hi_i32 v3, v3, s2
	v_lshrrev_b32_e32 v4, 31, v3
	v_lshrrev_b32_e32 v3, 7, v3
	v_add_u32_e32 v3, v3, v4
	v_lshl_or_b32 v1, v3, 20, v1
	v_add_u32_e32 v3, 0x1ec10, v2
	ds_write_b32 v3, v1

.LBB0_855:
	s_or_b64 exec, exec, s[0:1]
	s_waitcnt lgkmcnt(0)
	s_barrier
	s_getreg_b32 s0, hwreg(HW_REG_HW_ID, 0, 6)
	s_lshl_b32 s0, s0, 2
	s_add_i32 s0, s0, 0x27000
	v_mov_b32_e32 v0, s0
	ds_read_b32 v0, v0
	v_mov_b32_e32 v1, 0
	v_mov_b32_e32 v2, 0
	s_waitcnt lgkmcnt(0)
	v_readfirstlane_b32 s0, v0
	v_mbcnt_lo_u32_b32 v0, -1, v1
	v_mbcnt_hi_u32_b32 v0, -1, v0
	v_lshl_or_b32 v52, s0, 6, v0
	s_getreg_b32 s0, hwreg(HW_REG_HW_ID, 0, 6)
	s_lshl_b32 s0, s0, 2
	s_add_i32 s0, s0, 0x27000
	v_mov_b32_e32 v0, s0
	ds_read_b32 v0, v0
	v_mov_b32_e32 v1, 0
	s_waitcnt lgkmcnt(0)
	v_readfirstlane_b32 s0, v0
	v_mbcnt_lo_u32_b32 v0, -1, v2
	v_mbcnt_hi_u32_b32 v0, -1, v0
	v_lshl_or_b32 v0, s0, 6, v0
	s_movk_i32 s0, 0x100
	s_nop 0
	v_cmp_gt_i32_e32 vcc, s0, v0
	v_lshl_add_u32 v2, v0, 2, 0
	s_and_saveexec_b64 s[0:1], vcc
	s_cbranch_execz .LBB0_857
	v_ashrrev_i32_e32 v1, 31, v0
	v_lshlrev_b32_e32 v4, 6, v0
	v_and_b32_e32 v4, 0xffffff00, v4
	v_and_b32_e32 v5, 3, v0
	v_lshl_or_b32 v4, v5, 5, v4
	v_mov_b32_e32 v5, 0
	v_lshl_add_u64 v[4:5], v[4:5], 0, s[40:41]
	global_load_dword v1, v[4:5], off
	v_add_u32_e32 v3, 0x1e800, v2
	s_mov_b32 s2, 0x66666667
	s_waitcnt vmcnt(0)
	ds_write_b32 v3, v1
	v_add_u32_e32 v3, 0x13f, v1
	v_mul_hi_i32 v3, v3, s2
	v_lshrrev_b32_e32 v4, 31, v3
	v_lshrrev_b32_e32 v3, 7, v3
	v_add_u32_e32 v3, v3, v4
	v_lshl_or_b32 v1, v3, 20, v1
	v_add_u32_e32 v3, 0x1ec10, v2
	ds_write_b32 v3, v1

.LBB0_970:
	s_or_b64 exec, exec, s[0:1]
	s_waitcnt lgkmcnt(0)
	s_barrier
	s_getreg_b32 s0, hwreg(HW_REG_HW_ID, 0, 6)
	s_lshl_b32 s0, s0, 2
	s_add_i32 s0, s0, 0x27000
	v_mov_b32_e32 v0, s0
	ds_read_b32 v0, v0
	v_mov_b32_e32 v1, 0
	v_mov_b32_e32 v4, 0
	s_waitcnt lgkmcnt(0)
	v_readfirstlane_b32 s0, v0
	v_mbcnt_lo_u32_b32 v0, -1, v1
	v_mbcnt_hi_u32_b32 v0, -1, v0
	v_lshl_or_b32 v2, s0, 6, v0
	s_getreg_b32 s0, hwreg(HW_REG_HW_ID, 0, 6)
	s_lshl_b32 s0, s0, 2
	s_add_i32 s0, s0, 0x27000
	v_mov_b32_e32 v0, s0
	ds_read_b32 v0, v0
	v_mov_b32_e32 v1, 0
	s_waitcnt lgkmcnt(0)
	v_readfirstlane_b32 s0, v0
	v_mbcnt_lo_u32_b32 v0, -1, v1
	v_mbcnt_hi_u32_b32 v0, -1, v0
	v_lshl_or_b32 v3, s0, 6, v0
	s_getreg_b32 s0, hwreg(HW_REG_HW_ID, 0, 6)
	s_lshl_b32 s0, s0, 2
	s_add_i32 s0, s0, 0x27000
	v_mov_b32_e32 v0, s0
	ds_read_b32 v0, v0
	v_mov_b32_e32 v1, 0
	s_waitcnt lgkmcnt(0)
	v_readfirstlane_b32 s0, v0
	v_mbcnt_lo_u32_b32 v0, -1, v4
	v_mbcnt_hi_u32_b32 v0, -1, v0
	v_lshl_or_b32 v0, s0, 6, v0
	s_movk_i32 s0, 0x100
	s_nop 0
	v_cmp_gt_i32_e32 vcc, s0, v0
	v_lshl_add_u32 v4, v0, 2, 0
	s_and_saveexec_b64 s[0:1], vcc
	s_cbranch_execz .LBB0_972
	v_ashrrev_i32_e32 v1, 31, v0
	v_lshlrev_b32_e32 v6, 6, v0
	v_and_b32_e32 v6, 0xffffff00, v6
	v_and_b32_e32 v7, 3, v0
	v_lshl_or_b32 v6, v7, 5, v6
	v_mov_b32_e32 v7, 0
	v_lshl_add_u64 v[6:7], v[6:7], 0, s[40:41]
	global_load_dword v1, v[6:7], off
	v_add_u32_e32 v5, 0x1e800, v4
	s_mov_b32 s2, 0x66666667
	s_waitcnt vmcnt(0)
	ds_write_b32 v5, v1
	v_add_u32_e32 v5, 0x13f, v1
	v_mul_hi_i32 v5, v5, s2
	v_lshrrev_b32_e32 v6, 31, v5
	v_lshrrev_b32_e32 v5, 7, v5
	v_add_u32_e32 v5, v5, v6
	v_lshl_or_b32 v1, v5, 20, v1
	v_add_u32_e32 v5, 0x1ec10, v4
	ds_write_b32 v5, v1

.LBB0_2160:
	s_or_b64 exec, exec, s[0:1]
	s_waitcnt lgkmcnt(0)
	s_barrier
	s_add_u32 s30, s70, 0x9440
	s_getreg_b32 s0, hwreg(HW_REG_HW_ID, 0, 6)
	s_addc_u32 s31, s71, 0
	s_lshl_b32 s0, s0, 2
	s_add_i32 s0, s0, 0x27000
	v_mov_b32_e32 v0, s0
	ds_read_b32 v0, v0
	v_mov_b32_e32 v1, 0
	v_mov_b32_e32 v3, 0
	s_movk_i32 s33, 0x4000
	s_waitcnt lgkmcnt(0)
	v_readfirstlane_b32 s0, v0
	v_mbcnt_lo_u32_b32 v0, -1, v1
	v_mbcnt_hi_u32_b32 v0, -1, v0
	v_lshl_or_b32 v0, s0, 6, v0
	s_getreg_b32 s0, hwreg(HW_REG_HW_ID, 0, 6)
	s_lshl_b32 s0, s0, 2
	s_add_i32 s0, s0, 0x27000
	v_mov_b32_e32 v1, s0
	ds_read_b32 v2, v1
	v_mov_b32_e32 v1, 0
	s_waitcnt lgkmcnt(0)
	v_readfirstlane_b32 s0, v2
	v_mbcnt_lo_u32_b32 v2, -1, v3
	v_mbcnt_hi_u32_b32 v2, -1, v2
	v_lshl_or_b32 v2, s0, 6, v2
	v_readlane_b32 s0, v253, 30
	v_ashrrev_i32_e32 v8, 6, v2
	s_nop 0
	v_add_u32_e32 v2, s0, v8
	v_cmp_gt_i32_e32 vcc, s33, v2
	s_and_saveexec_b64 s[34:35], vcc
	s_cbranch_execz .LBB0_2249
	v_ashrrev_i32_e32 v3, 31, v2
	v_readlane_b32 s24, v253, 53
	v_and_b32_e32 v22, 63, v0
	v_lshlrev_b64 v[4:5], 10, v[2:3]
	v_readlane_b32 s25, v253, 54
	v_lshlrev_b32_e32 v0, 2, v22
	v_readlane_b32 s8, v253, 4
	v_lshl_add_u64 v[4:5], s[24:25], 0, v[4:5]
	v_lshl_add_u64 v[4:5], v[4:5], 0, v[0:1]
	global_load_dword v28, v[4:5], off
	global_load_dword v29, v[4:5], off offset:256
	global_load_dword v30, v[4:5], off offset:512
	global_load_dword v31, v[4:5], off offset:768
	v_readlane_b32 s9, v253, 5
	v_xor_b32_e32 v3, 64, v0
	v_xor_b32_e32 v23, 0x80, v0
	v_lshl_add_u64 v[4:5], s[8:9], 0, v[0:1]
	v_lshl_add_u64 v[6:7], s[24:25], 0, v[0:1]
	s_lshl_b32 s24, s72, 6
	v_lshlrev_b32_e32 v0, 3, v8
	v_readlane_b32 s10, v253, 6
	v_readlane_b32 s11, v253, 7
	v_readlane_b32 s12, v253, 8
	v_readlane_b32 s13, v253, 9
	v_readlane_b32 s14, v253, 10
	v_readlane_b32 s15, v253, 11
	v_readlane_b32 s16, v253, 12
	v_readlane_b32 s17, v253, 13
	v_readlane_b32 s18, v253, 14
	v_readlane_b32 s19, v253, 15
	v_readlane_b32 s20, v253, 16
	v_readlane_b32 s21, v253, 17
	v_readlane_b32 s22, v253, 18
	v_readlane_b32 s23, v253, 19
	v_add3_u32 v8, s24, v0, v22
	v_readlane_b32 s24, v253, 2
	v_cmp_gt_u32_e64 s[0:1], 32, v22
	v_cmp_lt_u32_e64 s[2:3], 31, v22
	v_cmp_lt_u32_e64 s[4:5], 7, v22
	v_cmp_gt_u32_e64 s[6:7], 8, v22
	v_cmp_eq_u32_e64 s[8:9], 0, v22
	v_cmp_eq_u32_e64 s[10:11], 1, v22
	v_cmp_eq_u32_e64 s[12:13], 2, v22
	v_cmp_eq_u32_e64 s[14:15], 3, v22
	v_cmp_eq_u32_e64 s[16:17], 4, v22
	v_cmp_eq_u32_e64 s[18:19], 5, v22
	v_cmp_eq_u32_e64 s[20:21], 6, v22
	v_cmp_eq_u32_e64 s[22:23], 7, v22
	s_lshl_b32 s42, s24, 6
	s_mov_b64 s[36:37], 0
	s_movk_i32 s43, 0x3fff
	s_mov_b32 s44, 0xbfb8aa3b
	s_mov_b32 s45, 0x42ce8ed0
	s_mov_b32 s46, 0xc2b17218
	v_mov_b32_e32 v24, 0x7f800000
	v_mov_b32_e32 v25, 0xff800000
	s_mov_b32 s47, 0xff800000
	v_mov_b32_e32 v26, 1
	v_readlane_b32 s25, v253, 3
	s_branch .LBB0_2163

.LBB0_2239:
	v_mov_b32_e32 v0, s48
	v_cndmask_b32_e64 v0, 0, v0, s[8:9]
	v_mov_b32_e32 v9, s49
	v_cndmask_b32_e64 v0, v0, v9, s[10:11]
	v_mov_b32_e32 v9, s50
	v_cndmask_b32_e64 v0, v0, v9, s[12:13]
	v_mov_b32_e32 v9, s51
	v_cndmask_b32_e64 v0, v0, v9, s[14:15]
	v_mov_b32_e32 v9, s52
	v_cndmask_b32_e64 v0, v0, v9, s[16:17]
	v_mov_b32_e32 v9, s53
	v_cndmask_b32_e64 v0, v0, v9, s[18:19]
	v_mov_b32_e32 v9, s54
	v_cndmask_b32_e64 v0, v0, v9, s[20:21]
	v_mov_b32_e32 v9, s55
	v_cndmask_b32_e64 v0, v0, v9, s[22:23]
	v_lshlrev_b32_e32 v9, 2, v0
	v_and_b32_e32 v9, 0xfc, v9
	ds_bpermute_b32 v12, v9, v12
	ds_bpermute_b32 v13, v9, v13
	ds_bpermute_b32 v11, v9, v11
	ds_bpermute_b32 v9, v9, v10
	v_lshrrev_b32_e32 v14, 6, v0
	v_cmp_eq_u32_e32 vcc, 2, v14
	s_waitcnt lgkmcnt(2)
	s_nop 0
	v_cndmask_b32_e32 v10, v13, v12, vcc
	v_cmp_eq_u32_e32 vcc, 1, v14
	s_waitcnt lgkmcnt(1)
	s_nop 0
	v_cndmask_b32_e32 v10, v10, v11, vcc
	v_cmp_gt_u32_e32 vcc, 64, v0
	s_waitcnt lgkmcnt(0)
	s_nop 0
	v_cndmask_b32_e32 v10, v10, v9, vcc
	v_cndmask_b32_e64 v9, v10, 0, s[4:5]
	s_nop 1
	v_add_f32_dpp v9, v9, v9 quad_perm:[1,0,3,2] row_mask:0xf bank_mask:0xf bound_ctrl:1
	s_nop 1
	v_add_f32_dpp v9, v9, v9 quad_perm:[2,3,0,1] row_mask:0xf bank_mask:0xf bound_ctrl:1
	s_nop 1
	v_mov_b32_dpp v11, v9 row_half_mirror row_mask:0xf bank_mask:0xf bound_ctrl:1
	s_and_saveexec_b64 s[26:27], s[6:7]
	s_cbranch_execz .LBB0_2162
	v_lshlrev_b32_e32 v12, 6, v0
	v_and_b32_e32 v12, 0xffffff00, v12
	v_and_b32_e32 v13, 3, v0
	v_lshl_or_b32 v12, v13, 5, v12
	v_mov_b32_e32 v13, 0
	v_lshl_add_u64 v[12:13], v[12:13], 0, s[30:31]
	global_atomic_add v12, v[12:13], v26, off sc0
	v_add_f32_e32 v11, v9, v11
	v_ashrrev_i32_e32 v9, 31, v8
	v_lshlrev_b64 v[16:17], 2, v[8:9]
	v_div_scale_f32 v9, s[28:29], v11, v11, v10
	v_rcp_f32_e32 v32, v9
	v_readlane_b32 s28, v253, 55
	v_readlane_b32 s29, v253, 56
	v_lshlrev_b64 v[14:15], 16, v[0:1]
	v_div_scale_f32 v13, vcc, v10, v11, v10
	v_lshl_add_u64 v[18:19], s[28:29], 0, v[16:17]
	global_store_dword v[18:19], v0, off
	v_fma_f32 v0, -v9, v32, 1.0
	v_readlane_b32 s28, v253, 59
	v_fmac_f32_e32 v32, v0, v32
	v_readlane_b32 s29, v253, 60
	v_mul_f32_e32 v0, v13, v32
	v_fma_f32 v18, -v9, v0, v13
	v_lshl_add_u64 v[20:21], s[28:29], 0, v[16:17]
	v_readlane_b32 s28, v253, 57
	v_readlane_b32 s29, v253, 58
	v_fmac_f32_e32 v0, v18, v32
	v_fma_f32 v9, -v9, v0, v13
	v_lshl_add_u64 v[16:17], s[28:29], 0, v[16:17]
	v_readlane_b32 s28, v253, 61
	v_div_fmas_f32 v0, v9, v32, v0
	v_readlane_b32 s29, v253, 62
	v_div_fixup_f32 v0, v0, v11, v10
	v_mul_f32_e32 v0, 0x40200000, v0
	v_lshl_add_u64 v[10:11], s[28:29], 0, v[14:15]
	global_store_dword v[16:17], v0, off
	s_waitcnt vmcnt(2)
	global_store_dword v[20:21], v12, off
	v_ashrrev_i32_e32 v13, 31, v12
	v_lshl_add_u64 v[10:11], v[12:13], 2, v[10:11]
	global_store_dword v[10:11], v2, off
	s_branch .LBB0_2162

.LBB0_2301:
	s_or_b64 exec, exec, s[0:1]
	s_waitcnt lgkmcnt(0)
	s_barrier
	s_getreg_b32 s0, hwreg(HW_REG_HW_ID, 0, 6)
	s_lshl_b32 s0, s0, 2
	s_add_i32 s0, s0, 0x27000
	v_mov_b32_e32 v0, s0
	ds_read_b32 v0, v0
	v_mov_b32_e32 v1, 0
	v_mov_b32_e32 v2, 0
	s_waitcnt lgkmcnt(0)
	v_readfirstlane_b32 s0, v0
	v_mbcnt_lo_u32_b32 v0, -1, v1
	v_mbcnt_hi_u32_b32 v0, -1, v0
	s_waitcnt vmcnt(9)
	v_lshl_or_b32 v52, s0, 6, v0
	s_getreg_b32 s0, hwreg(HW_REG_HW_ID, 0, 6)
	s_lshl_b32 s0, s0, 2
	s_add_i32 s0, s0, 0x27000
	v_mov_b32_e32 v0, s0
	ds_read_b32 v0, v0
	v_mov_b32_e32 v1, 0
	s_waitcnt lgkmcnt(0)
	v_readfirstlane_b32 s0, v0
	v_mbcnt_lo_u32_b32 v0, -1, v2
	v_mbcnt_hi_u32_b32 v0, -1, v0
	v_lshl_or_b32 v0, s0, 6, v0
	s_movk_i32 s0, 0x100
	s_nop 0
	v_cmp_gt_i32_e32 vcc, s0, v0
	v_lshl_add_u32 v2, v0, 2, 0
	s_and_saveexec_b64 s[0:1], vcc
	s_cbranch_execz .LBB0_2303
	v_ashrrev_i32_e32 v1, 31, v0
	v_lshlrev_b32_e32 v4, 6, v0
	v_and_b32_e32 v4, 0xffffff00, v4
	v_and_b32_e32 v5, 3, v0
	v_lshl_or_b32 v4, v5, 5, v4
	v_mov_b32_e32 v5, 0
	v_lshl_add_u64 v[4:5], v[4:5], 0, s[30:31]
	global_load_dword v1, v[4:5], off
	v_add_u32_e32 v3, 0x1e800, v2
	s_mov_b32 s2, 0x66666667
	s_waitcnt vmcnt(0)
	ds_write_b32 v3, v1
	v_add_u32_e32 v3, 0x13f, v1
	v_mul_hi_i32 v3, v3, s2
	v_lshrrev_b32_e32 v4, 31, v3
	v_lshrrev_b32_e32 v3, 7, v3
	v_add_u32_e32 v3, v3, v4
	v_lshl_or_b32 v1, v3, 20, v1
	v_add_u32_e32 v3, 0x1ec10, v2
	ds_write_b32 v3, v1

.LBB0_2435:
	s_or_b64 exec, exec, s[0:1]
	s_waitcnt lgkmcnt(0)
	s_barrier
	s_getreg_b32 s0, hwreg(HW_REG_HW_ID, 0, 6)
	s_lshl_b32 s0, s0, 2
	s_add_i32 s0, s0, 0x27000
	v_mov_b32_e32 v0, s0
	ds_read_b32 v0, v0
	v_mov_b32_e32 v1, 0
	v_mov_b32_e32 v2, 0
	s_waitcnt lgkmcnt(0)
	v_readfirstlane_b32 s0, v0
	v_mbcnt_lo_u32_b32 v0, -1, v1
	v_mbcnt_hi_u32_b32 v0, -1, v0
	v_lshl_or_b32 v52, s0, 6, v0
	s_getreg_b32 s0, hwreg(HW_REG_HW_ID, 0, 6)
	s_lshl_b32 s0, s0, 2
	s_add_i32 s0, s0, 0x27000
	v_mov_b32_e32 v0, s0
	ds_read_b32 v0, v0
	v_mov_b32_e32 v1, 0
	s_waitcnt lgkmcnt(0)
	v_readfirstlane_b32 s0, v0
	v_mbcnt_lo_u32_b32 v0, -1, v2
	v_mbcnt_hi_u32_b32 v0, -1, v0
	v_lshl_or_b32 v0, s0, 6, v0
	s_movk_i32 s0, 0x100
	s_nop 0
	v_cmp_gt_i32_e32 vcc, s0, v0
	v_lshl_add_u32 v2, v0, 2, 0
	s_and_saveexec_b64 s[0:1], vcc
	s_cbranch_execz .LBB0_2437
	v_ashrrev_i32_e32 v1, 31, v0
	v_lshlrev_b32_e32 v4, 6, v0
	v_and_b32_e32 v4, 0xffffff00, v4
	v_and_b32_e32 v5, 3, v0
	v_lshl_or_b32 v4, v5, 5, v4
	v_mov_b32_e32 v5, 0
	v_lshl_add_u64 v[4:5], v[4:5], 0, s[30:31]
	global_load_dword v1, v[4:5], off
	v_add_u32_e32 v3, 0x1e800, v2
	s_mov_b32 s2, 0x66666667
	s_waitcnt vmcnt(0)
	ds_write_b32 v3, v1
	v_add_u32_e32 v3, 0x13f, v1
	v_mul_hi_i32 v3, v3, s2
	v_lshrrev_b32_e32 v4, 31, v3
	v_lshrrev_b32_e32 v3, 7, v3
	v_add_u32_e32 v3, v3, v4
	v_lshl_or_b32 v1, v3, 20, v1
	v_add_u32_e32 v3, 0x1ec10, v2
	ds_write_b32 v3, v1

.LBB0_2549:
	s_or_b64 exec, exec, s[0:1]
	s_waitcnt lgkmcnt(0)
	s_barrier
	s_getreg_b32 s0, hwreg(HW_REG_HW_ID, 0, 6)
	s_lshl_b32 s0, s0, 2
	s_add_i32 s0, s0, 0x27000
	v_mov_b32_e32 v0, s0
	ds_read_b32 v0, v0
	v_mov_b32_e32 v1, 0
	v_mov_b32_e32 v4, 0
	s_waitcnt lgkmcnt(0)
	v_readfirstlane_b32 s0, v0
	v_mbcnt_lo_u32_b32 v0, -1, v1
	v_mbcnt_hi_u32_b32 v0, -1, v0
	v_lshl_or_b32 v2, s0, 6, v0
	s_getreg_b32 s0, hwreg(HW_REG_HW_ID, 0, 6)
	s_lshl_b32 s0, s0, 2
	s_add_i32 s0, s0, 0x27000
	v_mov_b32_e32 v0, s0
	ds_read_b32 v0, v0
	v_mov_b32_e32 v1, 0
	s_waitcnt lgkmcnt(0)
	v_readfirstlane_b32 s0, v0
	v_mbcnt_lo_u32_b32 v0, -1, v1
	v_mbcnt_hi_u32_b32 v0, -1, v0
	v_lshl_or_b32 v3, s0, 6, v0
	s_getreg_b32 s0, hwreg(HW_REG_HW_ID, 0, 6)
	s_lshl_b32 s0, s0, 2
	s_add_i32 s0, s0, 0x27000
	v_mov_b32_e32 v0, s0
	ds_read_b32 v0, v0
	v_mov_b32_e32 v1, 0
	s_waitcnt lgkmcnt(0)
	v_readfirstlane_b32 s0, v0
	v_mbcnt_lo_u32_b32 v0, -1, v4
	v_mbcnt_hi_u32_b32 v0, -1, v0
	v_lshl_or_b32 v0, s0, 6, v0
	s_movk_i32 s0, 0x100
	s_nop 0
	v_cmp_gt_i32_e32 vcc, s0, v0
	v_lshl_add_u32 v4, v0, 2, 0
	s_and_saveexec_b64 s[0:1], vcc
	s_cbranch_execz .LBB0_2551
	v_ashrrev_i32_e32 v1, 31, v0
	v_lshlrev_b32_e32 v6, 6, v0
	v_and_b32_e32 v6, 0xffffff00, v6
	v_and_b32_e32 v7, 3, v0
	v_lshl_or_b32 v6, v7, 5, v6
	v_mov_b32_e32 v7, 0
	v_lshl_add_u64 v[6:7], v[6:7], 0, s[30:31]
	global_load_dword v1, v[6:7], off
	v_add_u32_e32 v5, 0x1e800, v4
	s_mov_b32 s2, 0x66666667
	s_waitcnt vmcnt(0)
	ds_write_b32 v5, v1
	v_add_u32_e32 v5, 0x13f, v1
	v_mul_hi_i32 v5, v5, s2
	v_lshrrev_b32_e32 v6, 31, v5
	v_lshrrev_b32_e32 v5, 7, v5
	v_add_u32_e32 v5, v5, v6
	v_lshl_or_b32 v1, v5, 20, v1
	v_add_u32_e32 v5, 0x1ec10, v4
	ds_write_b32 v5, v1
